# nconv72 + last 128 in-proj tiles (gate_r cols) deferred to P2 on WGs>=128; P2 units rebalanced 6sp+5kv vs 2sp+3kv
# speedup vs baseline: 1.0121x; 1.0060x over previous
; #define SEAM(k) do { if (IN(k) && IN((k) + 1)) xcd_barrier(bar); } while (0)
; #define REP(k) for (int rep_ = reframe(F); rep_ < (((MK_DUP) >> (k)) & 1) + 1; ++rep_)
; #define REPBAR(k) do { if ((((MK_DUP) >> (k)) & 1) && rep_ == 0) xcd_barrier(bar); } while (0)
; __global__ void __launch_bounds__(NTHREADS, 2) mk_fwd(Args args) {
;     ...
;         if ((int)blockIdx.x < ngemm) {
;             pg8::DenseSched S; S.init((const bf16_t*)(F.ws + WS_H), D, (const bf16_t*)(F.ws + WS_WIN), D, T, INW, ngemm, (int)blockIdx.x);
;             EpiInProj E{F.ws};
;             if (MK_RSYNC) pg8::gemm_phase<0, EpiInProj, pg8::DenseSched, 127, 127, true>(F.lds, S, E, &bar); else pg8::gemm_phase<0>(F.lds, S, E);
;         } else if (!MK_CONV_IN_P0) conv_rest(F, args, ((int)blockIdx.x - ngemm) * NWAVES + F.wave, nconv * NWAVES);
;         REPBAR(1);
;     } SEAM(1);
;     if (IN(2)) REP(2) {
.LBB0_282:
	s_cmp_eq_u32 s101, 1
	s_cbranch_scc0 .Ldefer_norm
	s_mov_b32 s101, 2
	s_mov_b32 s92, s98
	s_ashr_i32 s93, s92, 31
	s_cmp_gt_i32 s89, 2
	s_cselect_b64 s[0:1], -1, 0
	s_branch .LBB0_336

; #define LAS __attribute__((address_space(3)))
; __device__ __forceinline__ unsigned cvt_pk_bf16(float lo, float hi) { f32x2 v = {lo, hi}; bf16x2_t b = __builtin_convertvector(v, bf16x2_t); return __builtin_bit_cast(unsigned, b); }
; #define REP(k) for (int rep_ = reframe(F); rep_ < (((MK_DUP) >> (k)) & 1) + 1; ++rep_)
; __device__ __forceinline__ void spatial_unit(Frame& F, const Args& a, int n, int g) {
;     LAS unsigned char* Wimg = F.lds; LAS unsigned char* Vimg = F.lds + 32768; LAS float* stats = (LAS float*)(F.lds + 65536);
;     const int t0 = n * 128, ch0 = g * 128, tid = F.tid, lane = F.lane, w = F.wave;
;     const bf16_t* V = (const bf16_t*)(F.ws + WS_V); const bf16_t* U = (const bf16_t*)(F.ws + WS_U); bf16_t* SG = (bf16_t*)(F.ws + WS_SG);
;     const float* vstat = (const float*)(F.ws + WS_VSTAT);
;     if (tid < 128) { const f32x4* p = (const f32x4*)(vstat + (size_t)(t0 + tid) * 32); float s = 0.f, q = 0.f;
; #pragma unroll
;         for (int j = 0; j < 8; ++j) { const f32x4 v = p[j]; s += v[0] + v[2]; q += v[1] + v[3]; }
;         const float mean = s * (1.f / GW), var = q * (1.f / GW) - mean * mean;
;         stats[2 * tid] = mean; stats[2 * tid + 1] = 1.0f / sqrtf(fmaxf(var, 0.f) + EPS); }
;     const float* ws_g = a.in[5] + (size_t)g * 128 * 128;
; #pragma unroll
;     for (int i = 0; i < 4; ++i) { const int id = tid + 512 * i, t = id >> 4, ch = id & 15;
;         const f32x4 x0 = *(const f32x4*)(ws_g + t * 128 + 8 * ch), x1 = *(const f32x4*)(ws_g + t * 128 + 8 * ch + 4);
;         float v[8] = {x0[0], x0[1], x0[2], x0[3], x1[0], x1[1], x1[2], x1[3]};
; #pragma unroll
;         for (int j = 0; j < 8; ++j) v[j] = (8 * ch + j <= t) ? v[j] : 0.f;
;         u32x4 o; o.x = cvt_pk_bf16(v[0], v[1]); o.y = cvt_pk_bf16(v[2], v[3]); o.z = cvt_pk_bf16(v[4], v[5]); o.w = cvt_pk_bf16(v[6], v[7]);
;         *(LAS u32x4*)(Wimg + off_b(t, ch)) = o; }
; __global__ void __launch_bounds__(NTHREADS, 2) mk_fwd(Args args) {
;     ...
;     if (IN(2)) REP(2) {
;         if (MK_NSCAN == 0) for (int u = blockIdx.x; u < 1024; u += F.G) spatial_unit(F, args, u >> 3, u & 7);
.LBB0_336:
	s_cmp_lt_i32 s88, 3
	s_cselect_b64 s[4:5], -1, 0
	s_and_b64 s[4:5], s[4:5], s[0:1]
	s_andn2_b64 vcc, exec, s[4:5]
	v_writelane_b32 v254, s88, 8
	s_nop 1
	v_writelane_b32 v254, s89, 9
	s_cbranch_vccnz .LBB0_353
	s_cmp_lg_u32 s101, 0
	s_cbranch_scc1 .Lp2_body
	s_cmpk_lt_i32 s92, 0x80
	s_cbranch_scc1 .Lp2_body
	s_add_i32 s92, s92, 0xb00
	s_movk_i32 s3, 128
	s_movk_i32 s99, 0xc00
	s_mov_b32 s101, 1
	s_branch .Lgemm_entry
.Lp2_body:
	s_waitcnt vmcnt(0)
	v_mov_b32_e32 v67, v0
	s_cmpk_gt_i32 s92, 0x3ff
	v_readfirstlane_b32 s0, v67
	s_cbranch_scc1 .LBB0_353
	v_ashrrev_i32_e32 v1, 4, v67
	v_lshlrev_b32_e32 v14, 2, v1
	v_and_b32_e32 v68, 15, v67
	v_and_b32_e32 v14, 12, v14
	v_bfe_u32 v78, v1, 2, 2
	v_bitop3_b32 v14, v14, v68, v78 bitop3:0x36
	v_lshl_add_u32 v81, v14, 4, 0
	v_add_u32_e32 v14, 0x200, v67
	v_ashrrev_i32_e32 v69, 4, v14
	v_lshlrev_b32_e32 v15, 2, v69
	v_and_b32_e32 v15, 12, v15
	v_bfe_u32 v16, v69, 2, 2
	v_bitop3_b32 v15, v15, v68, v16 bitop3:0x36
	v_add_u32_e32 v16, 0x400, v67
	v_ashrrev_i32_e32 v73, 4, v16
	v_lshlrev_b32_e32 v17, 2, v73
	s_load_dwordx8 s[72:79], s[96:97], 0x18
	v_and_b32_e32 v17, 12, v17
	v_bfe_u32 v18, v73, 2, 2
	v_bitop3_b32 v17, v17, v68, v18 bitop3:0x36
	v_add_u32_e32 v18, 0x600, v67
	v_lshlrev_b32_e32 v6, 3, v68
	v_ashrrev_i32_e32 v76, 4, v18
	v_mov_b32_e32 v2, 0
	v_cmp_gt_i32_e64 s[8:9], v6, v1
	v_cmp_lt_i32_e64 s[10:11], v6, v1
	v_or_b32_e32 v7, 2, v6
	v_or_b32_e32 v8, 3, v6
	v_or_b32_e32 v9, 4, v6
	v_or_b32_e32 v10, 5, v6
	v_or_b32_e32 v11, 6, v6
	v_or_b32_e32 v12, 7, v6
	v_cmp_gt_i32_e64 s[24:25], v6, v69
	v_cmp_lt_i32_e64 s[26:27], v6, v69
	v_cmp_gt_i32_e64 s[42:43], v6, v73
	v_cmp_lt_i32_e64 s[44:45], v6, v73
	v_cmp_gt_i32_e64 s[58:59], v6, v76
	v_cmp_lt_i32_e64 s[60:61], v6, v76
	v_lshlrev_b32_e32 v6, 2, v76
	s_waitcnt lgkmcnt(0)
; __device__ __forceinline__ void spatial_unit(Frame& F, const Args& a, int n, int g) {
;     ...
;     for (int i = 0; i < 4; ++i) { const int id = tid + 512 * i, t = id >> 4, ch = id & 15;
;         const f32x4 x0 = *(const f32x4*)(ws_g + t * 128 + 8 * ch), x1 = *(const f32x4*)(ws_g + t * 128 + 8 * ch + 4);
;         float v[8] = {x0[0], x0[1], x0[2], x0[3], x1[0], x1[1], x1[2], x1[3]};
; #pragma unroll
;         for (int j = 0; j < 8; ++j) v[j] = (8 * ch + j <= t) ? v[j] : 0.f;
;         u32x4 o; o.x = cvt_pk_bf16(v[0], v[1]); o.y = cvt_pk_bf16(v[2], v[3]); o.z = cvt_pk_bf16(v[4], v[5]); o.w = cvt_pk_bf16(v[6], v[7]);
;         *(LAS u32x4*)(Wimg + off_b(t, ch)) = o; }
;     __syncthreads();
;     const float* lng = a.in[3]; const float* lnb = a.in[4];
;     {
;         u32x4 xv[4]; const int ch = tid & 15;
; #pragma unroll
;         for (int i = 0; i < 4; ++i) xv[i] = __builtin_nontemporal_load((const u32x4*)(V + (size_t)(t0 + (tid >> 4) + 32 * i) * GW + ch0 + 8 * ch));
;         const f32x4 g0 = *(const f32x4*)(lng + ch0 + 8 * ch), g1 = *(const f32x4*)(lng + ch0 + 8 * ch + 4), b0 = *(const f32x4*)(lnb + ch0 + 8 * ch), b1 = *(const f32x4*)(lnb + ch0 + 8 * ch + 4);
; #pragma unroll
;         for (int i = 0; i < 4; ++i) { const int s = (tid >> 4) + 32 * i; const u32x4 x = xv[i];
;             const float mean = stats[2 * s], rstd = stats[2 * s + 1];
;             float v[8] = {bf_lo(x.x), bf_hi(x.x), bf_lo(x.y), bf_hi(x.y), bf_lo(x.z), bf_hi(x.z), bf_lo(x.w), bf_hi(x.w)};
; #pragma unroll
;             for (int j = 0; j < 4; ++j) { v[j] = (v[j] - mean) * rstd * g0[j] + b0[j]; v[4 + j] = (v[4 + j] - mean) * rstd * g1[j] + b1[j]; }
;             u32x4 o; o.x = cvt_pk_bf16(v[0], v[1]); o.y = cvt_pk_bf16(v[2], v[3]); o.z = cvt_pk_bf16(v[4], v[5]); o.w = cvt_pk_bf16(v[6], v[7]);
;             *(LAS u32x4*)(Vimg + off_b(s, ch)) = o; }
;     }
;     __syncthreads();
;     f32x4 acc[8];
; #pragma unroll
;     for (int c = 0; c < 8; ++c) acc[c] = (f32x4){0.f, 0.f, 0.f, 0.f};
;     const int ksmax = w >> 1;
;     {
;         unsigned vb[8][2];
; #pragma unroll
;         for (int c = 0; c < 8; ++c) { vb[c][0] = tr_base(lane, c, 0); vb[c][1] = tr_base(lane, c, 1); }
;         LAS unsigned char* Wrow = Wimg + 4096 * w;
; #pragma unroll
;         for (int ks = 0; ks < 4; ++ks) if (ks <= ksmax) {
;             const bf16x8 y = ROWF(Wrow, row_base(lane, ks), 0);
	v_lshlrev_b32_e32 v4, 5, v68
	v_mov_b32_e32 v5, v2
	v_cmp_gt_i32_e64 s[12:13], v7, v1
	v_cmp_gt_i32_e64 s[28:29], v7, v69
	v_cmp_gt_i32_e64 s[46:47], v7, v73
	v_cmp_gt_i32_e64 s[62:63], v7, v76
	v_and_b32_e32 v6, 12, v6
	v_bfe_u32 v7, v76, 2, 2
	v_and_b32_e32 v3, 63, v67
	v_lshl_add_u64 v[46:47], s[76:77], 0, v[4:5]
	v_cmp_gt_i32_e64 s[18:19], v10, v1
	v_cmp_gt_i32_e64 s[36:37], v10, v69
	v_cmp_gt_i32_e64 s[52:53], v10, v73
	v_cmp_gt_i32_e64 s[68:69], v10, v76
	v_bitop3_b32 v6, v6, v68, v7 bitop3:0x36
	v_lshlrev_b32_e32 v44, 4, v68
	v_mov_b32_e32 v45, v2
	v_lshl_add_u64 v[50:51], s[72:73], 0, v[4:5]
	v_lshl_add_u64 v[52:53], s[74:75], 0, v[4:5]
	v_bfe_u32 v5, v67, 2, 2
	v_bfe_u32 v10, v67, 1, 5
	v_lshlrev_b32_e32 v77, 3, v67
	v_cmp_gt_i32_e64 s[16:17], v9, v1
	v_cmp_gt_i32_e64 s[34:35], v9, v69
	v_cmp_gt_i32_e64 s[50:51], v9, v73
	v_cmp_gt_i32_e64 s[66:67], v9, v76
	v_lshl_add_u32 v9, v6, 4, 0
	v_lshl_add_u64 v[6:7], s[94:95], 0, v[44:45]
	v_and_b32_e32 v10, 24, v10
	v_bfe_u32 v45, v3, 1, 1
	v_lshlrev_b32_e32 v3, 2, v5
	v_lshrrev_b32_e32 v19, 3, v67
	v_or_b32_e32 v18, v10, v5
	v_and_or_b32 v79, v19, 2, v3
	v_and_b32_e32 v19, 8, v77
	v_or_b32_e32 v10, 4, v10
	v_lshl_or_b32 v72, v18, 8, v19
	v_or_b32_e32 v18, v10, v5
	v_bfe_u32 v10, v10, 2, 2
	v_lshl_or_b32 v75, v18, 8, v19
	v_or_b32_e32 v18, v79, v45
	v_lshl_or_b32 v89, v18, 4, v72
	v_bitop3_b32 v18, v10, v45, v3 bitop3:0x36
	v_lshl_or_b32 v90, v18, 4, v75
	v_or_b32_e32 v18, 2, v45
	v_bitop3_b32 v18, v10, v18, v3 bitop3:0x36
	v_lshl_or_b32 v92, v18, 4, v75
	v_or_b32_e32 v18, 4, v45
	v_bitop3_b32 v18, v10, v18, v3 bitop3:0x36
	v_lshl_or_b32 v94, v18, 4, v75
	v_or_b32_e32 v18, 6, v45
	v_bitop3_b32 v18, v10, v18, v3 bitop3:0x36
	v_lshl_or_b32 v96, v18, 4, v75
	v_or_b32_e32 v18, 8, v45
	v_bitop3_b32 v18, v10, v18, v3 bitop3:0x36
	s_ashr_i32 s3, s0, 6
	v_bitop3_b32 v19, v45, v79, 2 bitop3:0x36
	v_lshl_or_b32 v98, v18, 4, v75
	v_or_b32_e32 v18, 10, v45
	s_movk_i32 s1, 0x80
	s_add_u32 s80, s94, 0x50600000
	v_lshl_or_b32 v91, v19, 4, v72
	v_bitop3_b32 v19, v45, v79, 4 bitop3:0x36
	v_bitop3_b32 v18, v10, v18, v3 bitop3:0x36
	v_cmp_gt_i32_e64 s[6:7], s1, v67
	s_addc_u32 s81, s95, 0
	v_lshl_or_b32 v93, v19, 4, v72
	v_bitop3_b32 v19, v45, v79, 6 bitop3:0x36
	v_lshl_or_b32 v100, v18, 4, v75
	v_or_b32_e32 v18, 12, v45
	s_lshl_b32 s1, s3, 12
	v_lshl_or_b32 v95, v19, 4, v72
	v_bitop3_b32 v19, v45, v79, 8 bitop3:0x36
	v_bitop3_b32 v18, v10, v18, v3 bitop3:0x36
	s_ashr_i32 s0, s0, 7
	s_add_i32 s1, s1, 0
	v_lshl_or_b32 v97, v19, 4, v72
	v_bitop3_b32 v19, v45, v79, 10 bitop3:0x36
	v_lshl_or_b32 v102, v18, 4, v75
	v_or_b32_e32 v18, 14, v45
	s_cmp_gt_i32 s0, -1
	v_or_b32_e32 v80, v10, v3
	v_lshl_or_b32 v99, v19, 4, v72
	v_bitop3_b32 v19, v45, v79, 12 bitop3:0x36
	v_bitop3_b32 v3, v10, v18, v3 bitop3:0x36
	v_lshlrev_b32_e32 v10, 2, v67
	s_cselect_b64 s[74:75], -1, 0
	s_cmp_gt_i32 s0, 0
	v_lshl_or_b32 v101, v19, 4, v72
	v_bitop3_b32 v19, v45, v79, 14 bitop3:0x36
	v_lshl_or_b32 v104, v3, 4, v75
	v_bfe_u32 v3, v67, 4, 2
	v_and_b32_e32 v10, 12, v10
	s_cselect_b64 s[82:83], -1, 0
	s_cmp_gt_i32 s0, 1
	s_mov_b64 s[70:71], 0x3a600000
	v_lshl_or_b32 v103, v19, 4, v72
	v_lshl_add_u32 v18, v68, 8, s1
	v_bitop3_b32 v19, v10, v3, v5 bitop3:0x36
	v_or_b32_e32 v20, 4, v3
	s_cselect_b64 s[84:85], -1, 0
	v_or_b32_e32 v21, 8, v3
	s_cmp_gt_i32 s0, 2
	v_or_b32_e32 v3, 12, v3
	v_lshl_or_b32 v105, s3, 4, v68
	s_movk_i32 s33, 0x210
	s_mov_b64 s[0:1], 0x38600000
	v_writelane_b32 v254, s4, 10
	v_lshl_add_u64 v[48:49], v[6:7], 0, s[70:71]
	v_bitop3_b32 v20, v10, v20, v5 bitop3:0x36
	v_bitop3_b32 v21, v10, v21, v5 bitop3:0x36
	s_cselect_b64 s[86:87], -1, 0
	v_bitop3_b32 v3, v10, v3, v5 bitop3:0x36
	v_mul_lo_u32 v5, v105, s33
	s_add_i32 s70, 0, 0x10400
	v_lshl_add_u64 v[54:55], v[6:7], 0, s[0:1]
	s_mov_b64 s[0:1], 0x51000000
	v_writelane_b32 v254, s5, 11
	v_lshlrev_b32_e32 v36, 7, v1
	v_cmp_gt_i32_e64 s[14:15], v8, v1
	v_lshlrev_b32_e32 v13, 8, v1
	v_lshlrev_b32_e32 v38, 7, v69
	v_cmp_gt_i32_e64 s[30:31], v8, v69
	v_lshlrev_b32_e32 v14, 8, v69
	v_lshl_add_u32 v15, v15, 4, 0
	v_lshlrev_b32_e32 v40, 7, v73
	v_cmp_gt_i32_e64 s[48:49], v8, v73
	v_lshlrev_b32_e32 v16, 8, v73
	v_lshl_add_u32 v17, v17, 4, 0
	v_lshlrev_b32_e32 v42, 7, v76
	v_cmp_gt_i32_e64 s[64:65], v8, v76
	v_lshlrev_b32_e32 v8, 8, v76
	v_add_u32_e32 v84, 32, v1
	v_add_u32_e32 v83, 64, v1
	v_add_u32_e32 v82, 0x60, v1
	v_lshlrev_b32_e32 v19, 4, v19
	v_lshlrev_b32_e32 v20, 4, v20
	v_lshlrev_b32_e32 v21, 4, v21
	v_lshlrev_b32_e32 v3, 4, v3
	v_add_u32_e32 v5, s70, v5
	v_and_b32_e32 v10, 48, v67
	v_add_u32_e32 v4, s70, v4
	v_lshl_add_u64 v[56:57], v[6:7], 0, s[0:1]
	v_mul_lo_u32 v6, v1, s33
	s_lshl_b32 s33, s92, 4
	s_mov_b32 s0, s92
	v_ashrrev_i32_e32 v37, 31, v36
	v_cmp_gt_i32_e64 s[20:21], v11, v1
	v_cmp_gt_i32_e64 s[22:23], v12, v1
	s_mov_b32 s77, 0
	v_ashrrev_i32_e32 v39, 31, v38
	v_cmp_gt_i32_e64 s[38:39], v11, v69
	v_cmp_gt_i32_e64 s[40:41], v12, v69
	v_ashrrev_i32_e32 v41, 31, v40
	v_cmp_gt_i32_e64 s[54:55], v11, v73
	v_cmp_gt_i32_e64 s[56:57], v12, v73
	v_ashrrev_i32_e32 v43, 31, v42
	v_lshlrev_b32_e32 v85, 3, v1
	v_lshlrev_b32_e32 v86, 3, v84
	v_lshlrev_b32_e32 v70, 8, v84
	v_lshlrev_b32_e32 v87, 3, v83
	v_lshlrev_b32_e32 v71, 8, v83
	v_lshlrev_b32_e32 v88, 3, v82
	v_lshlrev_b32_e32 v74, 8, v82
	s_movk_i32 s4, 0x80
	s_movk_i32 s90, 0x800
	v_mov_b32_e32 v106, 0x260
	v_add_u32_e32 v107, v15, v14
	v_add_u32_e32 v108, v17, v16
	v_add_u32_e32 v109, v9, v8
	v_add_u32_e32 v110, v18, v19
	v_add_u32_e32 v111, v18, v20
	v_add_u32_e32 v112, v18, v21
	v_add_u32_e32 v113, v18, v3
	v_add_u32_e32 v114, v5, v10
	v_add_u32_e32 v115, v4, v6
	v_add_u32_e32 v66, v81, v13
	s_mov_b32 s91, s33
	v_writelane_b32 v254, s0, 12
	v_cmp_gt_i32_e64 s[70:71], v11, v76
	v_cmp_gt_i32_e64 s[72:73], v12, v76
	v_writelane_b32 v254, s1, 13
	s_movk_i32 s100, 0x300
	s_cmpk_lt_i32 s92, 0x80
	s_cbranch_scc1 .Lp2_sp_go
	s_movk_i32 s100, 0x400
	s_addk_i32 s92, 0x280
	s_lshl_b32 s91, s92, 4

; #define LAS __attribute__((address_space(3)))
; __device__ __forceinline__ unsigned cvt_pk_bf16(float lo, float hi) { f32x2 v = {lo, hi}; bf16x2_t b = __builtin_convertvector(v, bf16x2_t); return __builtin_bit_cast(unsigned, b); }
; __device__ __forceinline__ float bf_lo(unsigned w) { return __uint_as_float(w << 16); }
; __device__ __forceinline__ float bf_hi(unsigned w) { return __uint_as_float(w & 0xffff0000u); }
; __device__ __forceinline__ void spatial_unit(Frame& F, const Args& a, int n, int g) {
;     ...
;     {
;         LAS unsigned char* MT = F.lds + 66560;
;         const int t = 16 * w + (lane & 15); const float bias = a.in[6][g * 128 + t];
; #pragma unroll
;         for (int c = 0; c < 8; ++c) *(LAS f32x4*)(MT + t * 528 + (16 * c + 4 * (lane >> 4)) * 4) = acc[c] + bias;
;         __syncthreads();
;         u32x4 uu[4];
; #pragma unroll
;         for (int i = 0; i < 4; ++i) uu[i] = __builtin_nontemporal_load((const u32x4*)(U + (size_t)(t0 + (tid >> 4) + 32 * i) * GW + ch0 + 8 * (tid & 15)));
; #pragma unroll
;         for (int i = 0; i < 4; ++i) { const int tt = (tid >> 4) + 32 * i, ch = tid & 15;
;             const f32x4 m0 = *(const LAS f32x4*)(MT + tt * 528 + ch * 32), m1 = *(const LAS f32x4*)(MT + tt * 528 + ch * 32 + 16);
;             const u32x4 u4 = uu[i];
;             u32x4 r; r.x = cvt_pk_bf16(bf_lo(u4.x) * m0[0], bf_hi(u4.x) * m0[1]); r.y = cvt_pk_bf16(bf_lo(u4.y) * m0[2], bf_hi(u4.y) * m0[3]);
;             r.z = cvt_pk_bf16(bf_lo(u4.z) * m1[0], bf_hi(u4.z) * m1[1]); r.w = cvt_pk_bf16(bf_lo(u4.w) * m1[2], bf_hi(u4.w) * m1[3]);
;             *(u32x4*)(SG + (size_t)(t0 + tt) * GW + ch0 + 8 * ch) = r; }
;     }
;     __syncthreads();
; __global__ void __launch_bounds__(NTHREADS, 2) mk_fwd(Args args) {
;     ...
;         if (MK_NSCAN == 0) for (int u = blockIdx.x; u < 1024; u += F.G) spatial_unit(F, args, u >> 3, u & 7);
.LBB0_339:
	v_add_u32_e32 v132, s0, v105
	v_ashrrev_i32_e32 v133, 31, v132
	v_lshl_add_u64 v[132:133], v[132:133], 2, s[78:79]
	global_load_dword v132, v[132:133], off
	s_lshl_b32 s76, s0, 1
	s_add_i32 s92, s92, s4
	s_add_i32 s91, s91, s90
	s_cmp_lt_i32 s92, s100
	s_waitcnt vmcnt(0)
	v_pk_add_f32 v[6:7], v[6:7], v[132:133] op_sel_hi:[1,0]
	v_pk_add_f32 v[4:5], v[4:5], v[132:133] op_sel_hi:[1,0]
	ds_write_b128 v114, v[4:7] offset:448
	v_lshl_add_u64 v[4:5], v[54:55], 0, s[76:77]
	v_pk_add_f32 v[34:35], v[34:35], v[132:133] op_sel_hi:[1,0]
	v_pk_add_f32 v[32:33], v[32:33], v[132:133] op_sel_hi:[1,0]
	v_pk_add_f32 v[30:31], v[30:31], v[132:133] op_sel_hi:[1,0]
	v_pk_add_f32 v[28:29], v[28:29], v[132:133] op_sel_hi:[1,0]
	v_pk_add_f32 v[26:27], v[26:27], v[132:133] op_sel_hi:[1,0]
	v_pk_add_f32 v[24:25], v[24:25], v[132:133] op_sel_hi:[1,0]
	v_pk_add_f32 v[22:23], v[22:23], v[132:133] op_sel_hi:[1,0]
	v_pk_add_f32 v[20:21], v[20:21], v[132:133] op_sel_hi:[1,0]
	v_pk_add_f32 v[18:19], v[18:19], v[132:133] op_sel_hi:[1,0]
	v_pk_add_f32 v[16:17], v[16:17], v[132:133] op_sel_hi:[1,0]
	v_pk_add_f32 v[14:15], v[14:15], v[132:133] op_sel_hi:[1,0]
	v_pk_add_f32 v[12:13], v[12:13], v[132:133] op_sel_hi:[1,0]
	v_pk_add_f32 v[10:11], v[10:11], v[132:133] op_sel_hi:[1,0]
	v_pk_add_f32 v[8:9], v[8:9], v[132:133] op_sel_hi:[1,0]
	v_lshl_add_u64 v[6:7], v[4:5], 0, v[58:59]
	ds_write_b128 v114, v[32:35]
	ds_write_b128 v114, v[28:31] offset:64
	ds_write_b128 v114, v[24:27] offset:128
	ds_write_b128 v114, v[20:23] offset:192
	ds_write_b128 v114, v[16:19] offset:256
	ds_write_b128 v114, v[12:15] offset:320
	ds_write_b128 v114, v[8:11] offset:384
	s_waitcnt lgkmcnt(0)
	s_barrier
	global_load_dwordx4 v[10:13], v[6:7], off nt
	v_lshl_add_u64 v[6:7], v[4:5], 0, v[60:61]
	global_load_dwordx4 v[14:17], v[6:7], off nt
	v_lshl_add_u64 v[6:7], v[4:5], 0, v[62:63]
	global_load_dwordx4 v[18:21], v[6:7], off nt
	v_lshl_add_u64 v[4:5], v[4:5], 0, v[64:65]
	global_load_dwordx4 v[4:7], v[4:5], off nt
	ds_read_b128 v[22:25], v115
	ds_read_b128 v[26:29], v115 offset:16
	v_lshl_add_u64 v[8:9], v[56:57], 0, s[76:77]
	s_waitcnt vmcnt(3)
	v_lshlrev_b32_e32 v30, 16, v10
	v_and_b32_e32 v31, 0xffff0000, v10
	s_waitcnt lgkmcnt(1)
	v_pk_mul_f32 v[22:23], v[22:23], v[30:31]
	s_nop 0
	v_cvt_pk_bf16_f32 v10, v22, v23
	v_lshlrev_b32_e32 v22, 16, v11
	v_and_b32_e32 v23, 0xffff0000, v11
	v_pk_mul_f32 v[22:23], v[24:25], v[22:23]
	s_nop 0
	v_cvt_pk_bf16_f32 v11, v22, v23
	v_lshlrev_b32_e32 v22, 16, v12
	v_and_b32_e32 v23, 0xffff0000, v12
	s_waitcnt lgkmcnt(0)
	v_pk_mul_f32 v[22:23], v[26:27], v[22:23]
	s_waitcnt vmcnt(2)
	v_lshlrev_b32_e32 v26, 16, v14
	v_cvt_pk_bf16_f32 v12, v22, v23
	v_lshlrev_b32_e32 v22, 16, v13
	v_and_b32_e32 v23, 0xffff0000, v13
	v_pk_mul_f32 v[22:23], v[28:29], v[22:23]
	v_and_b32_e32 v27, 0xffff0000, v14
	v_cvt_pk_bf16_f32 v13, v22, v23
	v_lshl_add_u64 v[22:23], v[8:9], 0, v[58:59]
	global_store_dwordx4 v[22:23], v[10:13], off
	ds_read_b128 v[10:13], v115 offset:16896
	ds_read_b128 v[22:25], v115 offset:16912
	v_lshlrev_b32_e32 v14, 16, v15
	v_and_b32_e32 v15, 0xffff0000, v15
	s_waitcnt lgkmcnt(1)
	v_pk_mul_f32 v[10:11], v[10:11], v[26:27]
	v_pk_mul_f32 v[12:13], v[12:13], v[14:15]
	v_cvt_pk_bf16_f32 v10, v10, v11
	v_cvt_pk_bf16_f32 v11, v12, v13
	v_lshlrev_b32_e32 v12, 16, v16
	v_and_b32_e32 v13, 0xffff0000, v16
	v_lshlrev_b32_e32 v14, 16, v17
	v_and_b32_e32 v15, 0xffff0000, v17
	s_waitcnt lgkmcnt(0)
	v_pk_mul_f32 v[12:13], v[22:23], v[12:13]
	v_pk_mul_f32 v[14:15], v[24:25], v[14:15]
	v_cvt_pk_bf16_f32 v12, v12, v13
	v_cvt_pk_bf16_f32 v13, v14, v15
	v_add_u32_e32 v14, s93, v84
	v_ashrrev_i32_e32 v15, 31, v14
	v_lshlrev_b64 v[14:15], 11, v[14:15]
	v_lshl_add_u64 v[14:15], v[8:9], 0, v[14:15]
	global_store_dwordx4 v[14:15], v[10:13], off
	ds_read_b128 v[10:13], v115 offset:33792
	ds_read_b128 v[14:17], v115 offset:33808
	s_waitcnt vmcnt(3)
	v_lshlrev_b32_e32 v22, 16, v18
	v_and_b32_e32 v23, 0xffff0000, v18
	v_lshlrev_b32_e32 v18, 16, v19
	v_and_b32_e32 v19, 0xffff0000, v19
	s_waitcnt lgkmcnt(1)
	v_pk_mul_f32 v[10:11], v[10:11], v[22:23]
	v_pk_mul_f32 v[12:13], v[12:13], v[18:19]
	v_cvt_pk_bf16_f32 v10, v10, v11
	v_cvt_pk_bf16_f32 v11, v12, v13
	v_lshlrev_b32_e32 v12, 16, v20
	v_and_b32_e32 v13, 0xffff0000, v20
	s_waitcnt lgkmcnt(0)
	v_pk_mul_f32 v[12:13], v[14:15], v[12:13]
	v_lshlrev_b32_e32 v14, 16, v21
	v_and_b32_e32 v15, 0xffff0000, v21
	v_pk_mul_f32 v[14:15], v[16:17], v[14:15]
	v_cvt_pk_bf16_f32 v12, v12, v13
	v_cvt_pk_bf16_f32 v13, v14, v15
	v_add_u32_e32 v14, s93, v83
	v_ashrrev_i32_e32 v15, 31, v14
	v_lshlrev_b64 v[14:15], 11, v[14:15]
	v_lshl_add_u64 v[14:15], v[8:9], 0, v[14:15]
	global_store_dwordx4 v[14:15], v[10:13], off
	ds_read_b128 v[10:13], v115 offset:50688
	ds_read_b128 v[14:17], v115 offset:50704
	s_waitcnt vmcnt(3)
	v_lshlrev_b32_e32 v18, 16, v4
	v_and_b32_e32 v19, 0xffff0000, v4
	s_waitcnt lgkmcnt(1)
	v_pk_mul_f32 v[10:11], v[10:11], v[18:19]
	s_nop 0
	v_cvt_pk_bf16_f32 v4, v10, v11
	v_lshlrev_b32_e32 v10, 16, v5
	v_and_b32_e32 v11, 0xffff0000, v5
	v_pk_mul_f32 v[10:11], v[12:13], v[10:11]
	s_nop 0
	v_cvt_pk_bf16_f32 v5, v10, v11
	v_lshlrev_b32_e32 v10, 16, v6
	v_and_b32_e32 v11, 0xffff0000, v6
	s_waitcnt lgkmcnt(0)
	v_pk_mul_f32 v[10:11], v[14:15], v[10:11]
	s_nop 0
	v_cvt_pk_bf16_f32 v6, v10, v11
	v_lshlrev_b32_e32 v10, 16, v7
	v_and_b32_e32 v11, 0xffff0000, v7
	v_pk_mul_f32 v[10:11], v[16:17], v[10:11]
	s_nop 0
	v_cvt_pk_bf16_f32 v7, v10, v11
	v_add_u32_e32 v10, s93, v82
	v_ashrrev_i32_e32 v11, 31, v10
	v_lshlrev_b64 v[10:11], 11, v[10:11]
	v_lshl_add_u64 v[8:9], v[8:9], 0, v[10:11]
	global_store_dwordx4 v[8:9], v[4:7], off
	s_barrier
	s_cbranch_scc0 .LBB0_350

; #define LAS __attribute__((address_space(3)))
; __device__ __forceinline__ float bf_lo(unsigned w) { return __uint_as_float(w << 16); }
; __device__ __forceinline__ void kv_unit(Frame& F, const Args& a, int c, int h) {
;     LAS unsigned char* Kimg = F.lds; LAS unsigned char* Vimg = F.lds + 32768;
;     const int t0 = c * 128, tid = F.tid, lane = F.lane, w = F.wave;
;     const bf16_t* Kb = (const bf16_t*)(F.ws + WS_K); const bf16_t* RV = (const bf16_t*)(F.ws + WS_RV); float* KV = (float*)(F.ws + WS_KV);
;     const float l2g = a.l2g[h];
;     {
;         u32x4 kx[4], vx[8];
; #pragma unroll
;         for (int i = 0; i < 4; ++i) kx[i] = __builtin_nontemporal_load((const u32x4*)(Kb + (size_t)(t0 + (tid >> 4) + 32 * i) * QKW + h * 128 + 8 * (tid & 15)));
; #pragma unroll
;         for (int i = 0; i < 8; ++i) vx[i] = __builtin_nontemporal_load((const u32x4*)(RV + (size_t)(t0 + (tid >> 5) + 16 * i) * D + h * 256 + 8 * (tid & 31)));
; #pragma unroll
;         for (int i = 0; i < 4; ++i) *(LAS u32x4*)(Kimg + off_b((tid >> 4) + 32 * i, tid & 15)) = kx[i];
; #pragma unroll
;         for (int i = 0; i < 8; ++i) { const int s = (tid >> 5) + 16 * i, ch = tid & 31; const u32x4 x = vx[i]; const float z = exp2f((float)(127 - s) * l2g);
;             u32x4 o; o.x = cvt_pk_bf16(bf_lo(x.x) * z, bf_hi(x.x) * z); o.y = cvt_pk_bf16(bf_lo(x.y) * z, bf_hi(x.y) * z); o.z = cvt_pk_bf16(bf_lo(x.z) * z, bf_hi(x.z) * z); o.w = cvt_pk_bf16(bf_lo(x.w) * z, bf_hi(x.w) * z);
;             *(LAS u32x4*)(Vimg + (ch >> 4) * 32768 + off_b(s, ch & 15)) = o; }
;     }
;     __syncthreads();
;     f32x4 acc[2][8];
; #pragma unroll
;     for (int j = 0; j < 2; ++j)
; #pragma unroll
;         for (int cd = 0; cd < 8; ++cd) acc[j][cd] = (f32x4){0.f, 0.f, 0.f, 0.f};
;     LAS unsigned char* vi = Vimg + (w >> 2) * 32768; const int cimg = (2 * w) & 7;
;     {
;         unsigned kb[8][2], vb[2][2];
; #pragma unroll
;         for (int cd = 0; cd < 8; ++cd) { kb[cd][0] = tr_base(lane, cd, 0); kb[cd][1] = tr_base(lane, cd, 1); }
; #pragma unroll
;         for (int j = 0; j < 2; ++j) { vb[j][0] = tr_base(lane, cimg + j, 0); vb[j][1] = tr_base(lane, cimg + j, 1); }
; __global__ void __launch_bounds__(NTHREADS, 2) mk_fwd(Args args) {
;     ...
;         for (int u = blockIdx.x; u < 1024; u += F.G) kv_unit(F, args, u >> 3, u & 7);
.LBB0_350:
	v_and_b32_e32 v2, 0x78, v77
	v_lshlrev_b32_e32 v2, 1, v2
	v_mov_b32_e32 v3, 0
	v_lshl_add_u64 v[4:5], s[94:95], 0, v[2:3]
	v_and_b32_e32 v2, 0xf8, v77
	s_mov_b64 s[0:1], 0x3e600000
	v_lshlrev_b32_e32 v2, 1, v2
	v_lshl_add_u64 v[10:11], v[4:5], 0, s[0:1]
	v_lshl_add_u64 v[4:5], s[94:95], 0, v[2:3]
	s_mov_b64 s[0:1], 0x40600000
	v_lshl_add_u64 v[12:13], v[4:5], 0, s[0:1]
	v_lshlrev_b32_e32 v4, 2, v83
	v_and_b32_e32 v4, 12, v4
	v_bitop3_b32 v4, v4, v68, v78 bitop3:0x36
	v_lshl_add_u32 v51, v4, 4, 0
	v_lshlrev_b32_e32 v4, 2, v82
	v_ashrrev_i32_e32 v32, 5, v67
	v_and_b32_e32 v4, 12, v4
	v_bitop3_b32 v4, v4, v68, v78 bitop3:0x36
	v_sub_u32_e32 v6, 0x7f, v32
	v_lshl_add_u32 v54, v4, 4, 0
	v_lshlrev_b32_e32 v4, 11, v67
	v_cvt_f32_i32_e32 v33, v6
	v_lshlrev_b32_e32 v6, 2, v32
	v_and_b32_e32 v4, 0x8000, v4
	v_bfe_u32 v5, v32, 2, 2
	v_and_b32_e32 v6, 12, v6
	v_add_u32_e32 v4, 0, v4
	v_bitop3_b32 v6, v6, v68, v5 bitop3:0x36
	v_lshl_add_u32 v56, v6, 4, v4
	v_add_u32_e32 v6, 16, v32
	v_lshlrev_b32_e32 v57, 8, v6
	v_lshlrev_b32_e32 v6, 2, v6
	v_and_b32_e32 v6, 12, v6
	v_bitop3_b32 v6, v6, v68, v5 bitop3:0x36
	v_lshl_add_u32 v58, v6, 4, v4
	v_add_u32_e32 v6, 32, v32
	v_lshlrev_b32_e32 v59, 8, v6
	v_lshlrev_b32_e32 v6, 2, v6
	v_and_b32_e32 v6, 12, v6
	v_bitop3_b32 v6, v6, v68, v5 bitop3:0x36
	v_lshl_add_u32 v60, v6, 4, v4
	v_add_u32_e32 v6, 48, v32
	v_lshlrev_b32_e32 v61, 8, v6
	v_lshlrev_b32_e32 v6, 2, v6
	v_and_b32_e32 v6, 12, v6
	v_bitop3_b32 v6, v6, v68, v5 bitop3:0x36
	v_lshl_add_u32 v62, v6, 4, v4
	v_add_u32_e32 v6, 64, v32
	v_lshlrev_b32_e32 v63, 8, v6
	v_lshlrev_b32_e32 v6, 2, v6
	v_and_b32_e32 v6, 12, v6
	v_bitop3_b32 v6, v6, v68, v5 bitop3:0x36
	v_lshl_add_u32 v64, v6, 4, v4
	v_add_u32_e32 v6, 0x50, v32
	v_lshlrev_b32_e32 v65, 8, v6
	v_lshlrev_b32_e32 v6, 2, v6
	v_and_b32_e32 v6, 12, v6
	v_lshlrev_b32_e32 v2, 2, v84
	v_bitop3_b32 v6, v6, v68, v5 bitop3:0x36
	v_and_b32_e32 v2, 12, v2
	v_lshl_add_u32 v77, v6, 4, v4
	v_add_u32_e32 v6, 0x60, v32
	v_bitop3_b32 v2, v2, v68, v78 bitop3:0x36
	v_lshlrev_b32_e32 v78, 8, v6
	v_lshlrev_b32_e32 v6, 2, v6
	v_sub_u32_e32 v7, 0x6f, v32
	v_and_b32_e32 v6, 12, v6
	v_cvt_f32_i32_e32 v34, v7
	v_sub_u32_e32 v7, 0x5f, v32
	v_bitop3_b32 v6, v6, v68, v5 bitop3:0x36
	v_cvt_f32_i32_e32 v35, v7
	v_sub_u32_e32 v7, 0x4f, v32
	v_lshl_add_u32 v81, v6, 4, v4
	v_add_u32_e32 v6, 0x70, v32
	v_cvt_f32_i32_e32 v46, v7
	v_sub_u32_e32 v7, 63, v32
	v_lshlrev_b32_e32 v82, 8, v6
	v_lshlrev_b32_e32 v6, 2, v6
	v_cvt_f32_i32_e32 v47, v7
	v_sub_u32_e32 v7, 47, v32
	v_and_b32_e32 v6, 12, v6
	s_lshl_b32 s6, s3, 2
	v_cvt_f32_i32_e32 v48, v7
	v_sub_u32_e32 v7, 31, v32
	v_bitop3_b32 v5, v6, v68, v5 bitop3:0x36
	s_lshl_b32 s0, s3, 13
	s_and_b32 s6, s6, 12
	v_cvt_f32_i32_e32 v49, v7
	v_sub_u32_e32 v7, 15, v32
	v_lshl_add_u32 v83, v5, 4, v4
	s_and_b32 s0, s0, 0xffff8000
	v_or_b32_e32 v4, s6, v45
	v_cvt_f32_i32_e32 v50, v7
	v_bitop3_b32 v7, v4, v79, 2 bitop3:0x36
	v_bitop3_b32 v4, v80, v4, 2 bitop3:0x1e
	s_add_i32 s0, s0, 0
	v_lshl_add_u32 v85, v4, 4, s0
	v_lshrrev_b32_e32 v4, 1, v67
	v_bitop3_b32 v5, s6, v79, v45 bitop3:0x36
	v_bitop3_b32 v6, v80, s6, v45 bitop3:0x1e
	v_and_b32_e32 v4, 24, v4
	v_readlane_b32 s92, v254, 12
	s_movk_i32 s99, 0x280
	s_cmpk_lt_i32 s92, 0x80
	s_cbranch_scc1 .Lp2_kv_go
	s_movk_i32 s99, 0x400
	s_addk_i32 s92, 0x200
.Lp2_kv_go:
	s_lshl_b32 s33, s92, 4
	v_lshl_add_u32 v79, v5, 4, s0
	v_lshl_add_u32 v80, v6, 4, s0
	v_lshl_add_u32 v84, v7, 4, s0
	v_add_u32_e32 v86, 0, v4
	v_lshl_or_b32 v4, s3, 5, v68
	s_movk_i32 s0, 0x110
	v_readlane_b32 s93, v254, 13
	v_mul_lo_u32 v87, v4, s0
	v_add_u32_e32 v4, 0x800, v67
	v_add_u32_e32 v6, 0xa00, v67
	v_add_u32_e32 v8, 0xc00, v67
	v_add_u32_e32 v14, 0xe00, v67
	s_ashr_i32 s93, s92, 31
	v_ashrrev_i32_e32 v4, 4, v4
	v_ashrrev_i32_e32 v6, 4, v6
	v_ashrrev_i32_e32 v8, 4, v8
	v_ashrrev_i32_e32 v14, 4, v14
	s_lshl_b64 s[6:7], s[92:93], 16
	v_mul_lo_u32 v89, v4, s0
	v_lshlrev_b32_e32 v4, 7, v4
	v_mul_lo_u32 v90, v6, s0
	v_lshlrev_b32_e32 v6, 7, v6
	v_mul_lo_u32 v91, v8, s0
	v_lshlrev_b32_e32 v8, 7, v8
	v_lshlrev_b32_e32 v30, 7, v14
	s_add_u32 s6, s94, s6
	v_lshl_add_u32 v2, v2, 4, 0
	v_lshlrev_b32_e32 v55, 8, v32
	v_lshl_add_u32 v68, v68, 4, 0
	v_mul_lo_u32 v88, v1, s0
	v_mul_lo_u32 v69, v69, s0
	v_mul_lo_u32 v73, v73, s0
	v_mul_lo_u32 v76, v76, s0
	v_ashrrev_i32_e32 v5, 31, v4
	v_ashrrev_i32_e32 v7, 31, v6
	v_ashrrev_i32_e32 v9, 31, v8
	v_mul_lo_u32 v67, v14, s0
	v_ashrrev_i32_e32 v31, 31, v30
	v_mov_b64_e32 v[52:53], 0x53000000
	v_mov_b32_e32 v45, v3
	s_addc_u32 s7, s95, s7
	s_ashr_i32 s5, s4, 31
	s_mov_b32 s1, 0
	v_lshl_add_u64 v[14:15], v[36:37], 1, v[52:53]
	v_lshl_add_u64 v[16:17], s[6:7], 0, v[44:45]
	s_lshl_b64 s[6:7], s[4:5], 16
	v_lshl_add_u64 v[18:19], v[38:39], 1, v[52:53]
	v_lshl_add_u64 v[20:21], v[40:41], 1, v[52:53]
	v_lshl_add_u64 v[22:23], v[42:43], 1, v[52:53]
	v_lshl_add_u64 v[24:25], v[4:5], 1, v[52:53]
	v_lshl_add_u64 v[26:27], v[6:7], 1, v[52:53]
	v_lshl_add_u64 v[28:29], v[8:9], 1, v[52:53]
	v_lshl_add_u64 v[30:31], v[30:31], 1, v[52:53]
	s_mov_b32 s3, 0x10000
	s_mov_b32 s8, 0x20000
	s_mov_b32 s9, 0x30000
	s_mov_b32 s10, 0x40000
	s_mov_b32 s11, 0x50000
	s_mov_b32 s12, 0x60000
	s_mov_b32 s13, 0x70000
	v_add_u32_e32 v36, v2, v70
	v_add_u32_e32 v37, v51, v71
	v_add_u32_e32 v38, v54, v74
	s_mov_b32 s14, 0xc2fc0000
	v_add_u32_e32 v39, v56, v55
	v_add_u32_e32 v40, v58, v57
	v_add_u32_e32 v41, v60, v59
	v_add_u32_e32 v42, v62, v61
	v_add_u32_e32 v43, v64, v63
	v_add_u32_e32 v44, v77, v65
	v_add_u32_e32 v45, v81, v78
	v_add_u32_e32 v51, v83, v82
	v_add_u32_e32 v52, v79, v72
	v_add_u32_e32 v53, v80, v75
	v_add_u32_e32 v54, v84, v72
	v_add_u32_e32 v55, v85, v75
	v_add_u32_e32 v56, v86, v87
	v_add_u32_e32 v57, v68, v88
	v_add_u32_e32 v58, v68, v69
	v_add_u32_e32 v59, v68, v73
	v_add_u32_e32 v60, v68, v76
	v_add_u32_e32 v61, v68, v89
	v_add_u32_e32 v62, v68, v90
	v_add_u32_e32 v63, v68, v91
	v_add_u32_e32 v64, v68, v67
	v_mov_b32_e32 v65, 0x42800000
	v_not_b32_e32 v67, 63
	s_mov_b32 s15, s92
; #define LAS __attribute__((address_space(3)))
; __device__ __forceinline__ unsigned cvt_pk_bf16(float lo, float hi) { f32x2 v = {lo, hi}; bf16x2_t b = __builtin_convertvector(v, bf16x2_t); return __builtin_bit_cast(unsigned, b); }
; __device__ __forceinline__ float bf_lo(unsigned w) { return __uint_as_float(w << 16); }
; __device__ __forceinline__ float bf_hi(unsigned w) { return __uint_as_float(w & 0xffff0000u); }
; __device__ __forceinline__ void kv_unit(Frame& F, const Args& a, int c, int h) {
;     ...
;     const float l2g = a.l2g[h];
;     {
;         u32x4 kx[4], vx[8];
; #pragma unroll
;         for (int i = 0; i < 4; ++i) kx[i] = __builtin_nontemporal_load((const u32x4*)(Kb + (size_t)(t0 + (tid >> 4) + 32 * i) * QKW + h * 128 + 8 * (tid & 15)));
; #pragma unroll
;         for (int i = 0; i < 8; ++i) vx[i] = __builtin_nontemporal_load((const u32x4*)(RV + (size_t)(t0 + (tid >> 5) + 16 * i) * D + h * 256 + 8 * (tid & 31)));
; #pragma unroll
;         for (int i = 0; i < 4; ++i) *(LAS u32x4*)(Kimg + off_b((tid >> 4) + 32 * i, tid & 15)) = kx[i];
; #pragma unroll
;         for (int i = 0; i < 8; ++i) { const int s = (tid >> 5) + 16 * i, ch = tid & 31; const u32x4 x = vx[i]; const float z = exp2f((float)(127 - s) * l2g);
;             u32x4 o; o.x = cvt_pk_bf16(bf_lo(x.x) * z, bf_hi(x.x) * z); o.y = cvt_pk_bf16(bf_lo(x.y) * z, bf_hi(x.y) * z); o.z = cvt_pk_bf16(bf_lo(x.z) * z, bf_hi(x.z) * z); o.w = cvt_pk_bf16(bf_lo(x.w) * z, bf_hi(x.w) * z);
;             *(LAS u32x4*)(Vimg + (ch >> 4) * 32768 + off_b(s, ch & 15)) = o; }
.LBB0_351:
	s_and_b32 s17, s33, 0xffffff80
	s_and_b32 s16, s15, 7
	v_add_u32_e32 v2, s17, v1
	s_lshl_b32 s0, s16, 8
	v_ashrrev_i32_e32 v3, 31, v2
	v_add_u32_e32 v6, s17, v32
	v_lshl_add_u64 v[4:5], v[10:11], 0, s[0:1]
	v_lshlrev_b64 v[2:3], 11, v[2:3]
	s_lshl_b32 s0, s16, 9
	v_ashrrev_i32_e32 v7, 31, v6
	v_lshl_add_u64 v[2:3], v[4:5], 0, v[2:3]
	v_lshl_add_u64 v[8:9], v[12:13], 0, s[0:1]
	v_lshlrev_b64 v[6:7], 12, v[6:7]
	v_add_co_u32_e32 v4, vcc, s3, v2
	v_lshl_add_u64 v[6:7], v[8:9], 0, v[6:7]
	s_nop 0
	v_addc_co_u32_e32 v5, vcc, 0, v3, vcc
	global_load_dwordx4 v[68:71], v[2:3], off nt
	global_load_dwordx4 v[72:75], v[4:5], off nt
	global_load_dwordx4 v[76:79], v[6:7], off nt
	v_add_co_u32_e32 v4, vcc, s8, v2
	s_lshl_b32 s0, s16, 2
	s_nop 0
	v_addc_co_u32_e32 v5, vcc, 0, v3, vcc
	v_add_co_u32_e32 v2, vcc, s9, v2
	s_nop 1
	v_addc_co_u32_e32 v3, vcc, 0, v3, vcc
	global_load_dwordx4 v[80:83], v[4:5], off nt
	global_load_dwordx4 v[84:87], v[2:3], off nt
	v_add_co_u32_e32 v2, vcc, s3, v6
	s_load_dword s0, s[96:97], s0 offset:0xa0
	s_nop 0
	v_addc_co_u32_e32 v3, vcc, 0, v7, vcc
	global_load_dwordx4 v[88:91], v[2:3], off nt
	v_add_co_u32_e32 v2, vcc, s8, v6
	s_nop 1
	v_addc_co_u32_e32 v3, vcc, 0, v7, vcc
	global_load_dwordx4 v[92:95], v[2:3], off nt
	v_add_co_u32_e32 v4, vcc, s9, v6
	s_nop 1
	v_addc_co_u32_e32 v5, vcc, 0, v7, vcc
	v_add_co_u32_e32 v2, vcc, s10, v6
	s_nop 1
	v_addc_co_u32_e32 v3, vcc, 0, v7, vcc
	v_add_co_u32_e32 v8, vcc, s11, v6
	s_nop 1
	v_addc_co_u32_e32 v9, vcc, 0, v7, vcc
	global_load_dwordx4 v[96:99], v[4:5], off nt
	global_load_dwordx4 v[100:103], v[2:3], off nt
	global_load_dwordx4 v[104:107], v[8:9], off nt
	v_add_co_u32_e32 v108, vcc, s12, v6
	s_waitcnt lgkmcnt(0)
	v_mul_f32_e32 v2, s0, v33
	v_addc_co_u32_e32 v109, vcc, 0, v7, vcc
	v_add_co_u32_e32 v110, vcc, s13, v6
	s_nop 1
	v_addc_co_u32_e32 v111, vcc, 0, v7, vcc
	v_cmp_gt_f32_e32 vcc, s14, v2
	s_nop 1
	v_cndmask_b32_e32 v2, 0, v65, vcc
	v_fmac_f32_e32 v2, s0, v33
	v_exp_f32_e32 v112, v2
	global_load_dwordx4 v[6:9], v[108:109], off nt
	global_load_dwordx4 v[2:5], v[110:111], off nt
	v_cndmask_b32_e32 v108, 0, v67, vcc
	v_ldexp_f32 v108, v112, v108
	s_waitcnt vmcnt(11)
	ds_write_b128 v66, v[68:71]
	s_waitcnt vmcnt(10)
	ds_write_b128 v36, v[72:75]
	s_waitcnt vmcnt(9)
	v_lshlrev_b32_e32 v68, 16, v76
	v_and_b32_e32 v69, 0xffff0000, v76
	v_lshlrev_b32_e32 v70, 16, v77
	v_and_b32_e32 v71, 0xffff0000, v77
	v_pk_mul_f32 v[68:69], v[108:109], v[68:69] op_sel_hi:[0,1]
	v_pk_mul_f32 v[70:71], v[108:109], v[70:71] op_sel_hi:[0,1]
	v_cvt_pk_bf16_f32 v68, v68, v69
	v_cvt_pk_bf16_f32 v69, v70, v71
	v_lshlrev_b32_e32 v70, 16, v78
	v_and_b32_e32 v71, 0xffff0000, v78
	v_pk_mul_f32 v[70:71], v[108:109], v[70:71] op_sel_hi:[0,1]
	v_cvt_pk_bf16_f32 v70, v70, v71
	v_mul_f32_e32 v71, s0, v34
	v_cmp_gt_f32_e32 vcc, s14, v71
	v_lshlrev_b32_e32 v72, 16, v79
	v_and_b32_e32 v73, 0xffff0000, v79
	v_cndmask_b32_e32 v71, 0, v65, vcc
	v_fmac_f32_e32 v71, s0, v34
	v_exp_f32_e32 v74, v71
	v_pk_mul_f32 v[72:73], v[108:109], v[72:73] op_sel_hi:[0,1]
	v_cvt_pk_bf16_f32 v71, v72, v73
	s_waitcnt vmcnt(8)
	ds_write_b128 v37, v[80:83]
	s_waitcnt vmcnt(7)
	ds_write_b128 v38, v[84:87]
	ds_write_b128 v39, v[68:71] offset:32768
	v_cndmask_b32_e32 v68, 0, v67, vcc
	v_ldexp_f32 v72, v74, v68
	s_waitcnt vmcnt(6)
	v_lshlrev_b32_e32 v68, 16, v88
	v_and_b32_e32 v69, 0xffff0000, v88
	v_lshlrev_b32_e32 v70, 16, v89
	v_and_b32_e32 v71, 0xffff0000, v89
	v_pk_mul_f32 v[68:69], v[72:73], v[68:69] op_sel_hi:[0,1]
	v_pk_mul_f32 v[70:71], v[72:73], v[70:71] op_sel_hi:[0,1]
	v_cvt_pk_bf16_f32 v68, v68, v69
	v_cvt_pk_bf16_f32 v69, v70, v71
	v_lshlrev_b32_e32 v70, 16, v90
	v_and_b32_e32 v71, 0xffff0000, v90
	v_pk_mul_f32 v[70:71], v[72:73], v[70:71] op_sel_hi:[0,1]
	v_cvt_pk_bf16_f32 v70, v70, v71
	v_mul_f32_e32 v71, s0, v35
	v_cmp_gt_f32_e32 vcc, s14, v71
	v_lshlrev_b32_e32 v74, 16, v91
	v_and_b32_e32 v75, 0xffff0000, v91
	v_cndmask_b32_e32 v71, 0, v65, vcc
	v_fmac_f32_e32 v71, s0, v35
	v_pk_mul_f32 v[72:73], v[72:73], v[74:75] op_sel_hi:[0,1]
	v_exp_f32_e32 v74, v71
	v_cvt_pk_bf16_f32 v71, v72, v73
	ds_write_b128 v40, v[68:71] offset:32768
	v_cndmask_b32_e32 v68, 0, v67, vcc
	v_ldexp_f32 v72, v74, v68
	s_waitcnt vmcnt(5)
	v_lshlrev_b32_e32 v68, 16, v92
	v_and_b32_e32 v69, 0xffff0000, v92
	v_lshlrev_b32_e32 v70, 16, v93
	v_and_b32_e32 v71, 0xffff0000, v93
	v_pk_mul_f32 v[68:69], v[72:73], v[68:69] op_sel_hi:[0,1]
	v_pk_mul_f32 v[70:71], v[72:73], v[70:71] op_sel_hi:[0,1]
	v_cvt_pk_bf16_f32 v68, v68, v69
	v_cvt_pk_bf16_f32 v69, v70, v71
	v_lshlrev_b32_e32 v70, 16, v94
	v_and_b32_e32 v71, 0xffff0000, v94
	v_pk_mul_f32 v[70:71], v[72:73], v[70:71] op_sel_hi:[0,1]
	v_cvt_pk_bf16_f32 v70, v70, v71
	v_mul_f32_e32 v71, s0, v46
	v_cmp_gt_f32_e32 vcc, s14, v71
	v_lshlrev_b32_e32 v74, 16, v95
	v_and_b32_e32 v75, 0xffff0000, v95
	v_cndmask_b32_e32 v71, 0, v65, vcc
	v_fmac_f32_e32 v71, s0, v46
	v_pk_mul_f32 v[72:73], v[72:73], v[74:75] op_sel_hi:[0,1]
	v_exp_f32_e32 v74, v71
	v_cvt_pk_bf16_f32 v71, v72, v73
	ds_write_b128 v41, v[68:71] offset:32768
	v_cndmask_b32_e32 v68, 0, v67, vcc
	v_ldexp_f32 v72, v74, v68
	s_waitcnt vmcnt(4)
	v_lshlrev_b32_e32 v68, 16, v96
	v_and_b32_e32 v69, 0xffff0000, v96
	v_lshlrev_b32_e32 v70, 16, v97
	v_and_b32_e32 v71, 0xffff0000, v97
	v_pk_mul_f32 v[68:69], v[72:73], v[68:69] op_sel_hi:[0,1]
	v_pk_mul_f32 v[70:71], v[72:73], v[70:71] op_sel_hi:[0,1]
	v_cvt_pk_bf16_f32 v68, v68, v69
	v_cvt_pk_bf16_f32 v69, v70, v71
	v_lshlrev_b32_e32 v70, 16, v98
	v_and_b32_e32 v71, 0xffff0000, v98
	v_pk_mul_f32 v[70:71], v[72:73], v[70:71] op_sel_hi:[0,1]
	v_cvt_pk_bf16_f32 v70, v70, v71
	v_mul_f32_e32 v71, s0, v47
	v_cmp_gt_f32_e32 vcc, s14, v71
	v_lshlrev_b32_e32 v74, 16, v99
	v_and_b32_e32 v75, 0xffff0000, v99
	v_cndmask_b32_e32 v71, 0, v65, vcc
	v_fmac_f32_e32 v71, s0, v47
	v_pk_mul_f32 v[72:73], v[72:73], v[74:75] op_sel_hi:[0,1]
	v_exp_f32_e32 v74, v71
	v_cvt_pk_bf16_f32 v71, v72, v73
	ds_write_b128 v42, v[68:71] offset:32768
	v_cndmask_b32_e32 v68, 0, v67, vcc
	v_ldexp_f32 v72, v74, v68
	s_waitcnt vmcnt(3)
; #define LAS __attribute__((address_space(3)))
; __device__ __forceinline__ unsigned cvt_pk_bf16(float lo, float hi) { f32x2 v = {lo, hi}; bf16x2_t b = __builtin_convertvector(v, bf16x2_t); return __builtin_bit_cast(unsigned, b); }
; __device__ __forceinline__ float bf_lo(unsigned w) { return __uint_as_float(w << 16); }
; __device__ __forceinline__ float bf_hi(unsigned w) { return __uint_as_float(w & 0xffff0000u); }
; #define MFMA16(a, b, c) __builtin_amdgcn_mfma_f32_16x16x32_bf16(a, b, c, 0, 0, 0)
; __device__ __forceinline__ unsigned tr_base(unsigned lane, unsigned c, unsigned t) { return tr_addr16(lane, c, 0, t); }
; __device__ __forceinline__ void kv_unit(Frame& F, const Args& a, int c, int h) {
;     ...
;         for (int i = 0; i < 8; ++i) { const int s = (tid >> 5) + 16 * i, ch = tid & 31; const u32x4 x = vx[i]; const float z = exp2f((float)(127 - s) * l2g);
;             u32x4 o; o.x = cvt_pk_bf16(bf_lo(x.x) * z, bf_hi(x.x) * z); o.y = cvt_pk_bf16(bf_lo(x.y) * z, bf_hi(x.y) * z); o.z = cvt_pk_bf16(bf_lo(x.z) * z, bf_hi(x.z) * z); o.w = cvt_pk_bf16(bf_lo(x.w) * z, bf_hi(x.w) * z);
;             *(LAS u32x4*)(Vimg + (ch >> 4) * 32768 + off_b(s, ch & 15)) = o; }
;     }
;     __syncthreads();
;     f32x4 acc[2][8];
; #pragma unroll
;     for (int j = 0; j < 2; ++j)
; #pragma unroll
;         for (int cd = 0; cd < 8; ++cd) acc[j][cd] = (f32x4){0.f, 0.f, 0.f, 0.f};
;     LAS unsigned char* vi = Vimg + (w >> 2) * 32768; const int cimg = (2 * w) & 7;
;     {
;         unsigned kb[8][2], vb[2][2];
; #pragma unroll
;         for (int cd = 0; cd < 8; ++cd) { kb[cd][0] = tr_base(lane, cd, 0); kb[cd][1] = tr_base(lane, cd, 1); }
; #pragma unroll
;         for (int j = 0; j < 2; ++j) { vb[j][0] = tr_base(lane, cimg + j, 0); vb[j][1] = tr_base(lane, cimg + j, 1); }
; #pragma unroll
;         for (int ks = 0; ks < 4; ++ks) {
;             const bf16x8 y0 = trf(vi, vb[0][0], vb[0][1], 8192 * ks), y1 = trf(vi, vb[1][0], vb[1][1], 8192 * ks);
;             bf16x8 xf[8];
; #pragma unroll
;             for (int cd = 0; cd < 8; ++cd) xf[cd] = trf(Kimg, kb[cd][0], kb[cd][1], 8192 * ks);
;             __builtin_amdgcn_sched_barrier(0);
; #pragma unroll
;             for (int cd = 0; cd < 8; ++cd) { acc[0][cd] = MFMA16(xf[cd], y0, acc[0][cd]); acc[1][cd] = MFMA16(xf[cd], y1, acc[1][cd]); }
;             __builtin_amdgcn_sched_barrier(0);
;         }
	v_lshlrev_b32_e32 v68, 16, v100
	v_and_b32_e32 v69, 0xffff0000, v100
	v_lshlrev_b32_e32 v70, 16, v101
	v_and_b32_e32 v71, 0xffff0000, v101
	v_pk_mul_f32 v[68:69], v[72:73], v[68:69] op_sel_hi:[0,1]
	v_pk_mul_f32 v[70:71], v[72:73], v[70:71] op_sel_hi:[0,1]
	v_cvt_pk_bf16_f32 v68, v68, v69
	v_cvt_pk_bf16_f32 v69, v70, v71
	v_lshlrev_b32_e32 v70, 16, v102
	v_and_b32_e32 v71, 0xffff0000, v102
	v_pk_mul_f32 v[70:71], v[72:73], v[70:71] op_sel_hi:[0,1]
	v_cvt_pk_bf16_f32 v70, v70, v71
	v_mul_f32_e32 v71, s0, v48
	v_cmp_gt_f32_e32 vcc, s14, v71
	v_lshlrev_b32_e32 v74, 16, v103
	v_and_b32_e32 v75, 0xffff0000, v103
	v_cndmask_b32_e32 v71, 0, v65, vcc
	v_fmac_f32_e32 v71, s0, v48
	v_pk_mul_f32 v[72:73], v[72:73], v[74:75] op_sel_hi:[0,1]
	v_exp_f32_e32 v74, v71
	v_cvt_pk_bf16_f32 v71, v72, v73
	ds_write_b128 v43, v[68:71] offset:32768
	v_cndmask_b32_e32 v68, 0, v67, vcc
	v_ldexp_f32 v72, v74, v68
	s_waitcnt vmcnt(2)
	v_lshlrev_b32_e32 v68, 16, v104
	v_and_b32_e32 v69, 0xffff0000, v104
	v_lshlrev_b32_e32 v70, 16, v105
	v_and_b32_e32 v71, 0xffff0000, v105
	v_pk_mul_f32 v[68:69], v[72:73], v[68:69] op_sel_hi:[0,1]
	v_pk_mul_f32 v[70:71], v[72:73], v[70:71] op_sel_hi:[0,1]
	v_cvt_pk_bf16_f32 v68, v68, v69
	v_cvt_pk_bf16_f32 v69, v70, v71
	v_lshlrev_b32_e32 v70, 16, v106
	v_and_b32_e32 v71, 0xffff0000, v106
	v_pk_mul_f32 v[70:71], v[72:73], v[70:71] op_sel_hi:[0,1]
	v_cvt_pk_bf16_f32 v70, v70, v71
	v_mul_f32_e32 v71, s0, v49
	v_cmp_gt_f32_e32 vcc, s14, v71
	v_lshlrev_b32_e32 v74, 16, v107
	v_and_b32_e32 v75, 0xffff0000, v107
	v_cndmask_b32_e32 v71, 0, v65, vcc
	v_fmac_f32_e32 v71, s0, v49
	v_pk_mul_f32 v[72:73], v[72:73], v[74:75] op_sel_hi:[0,1]
	v_exp_f32_e32 v74, v71
	v_cvt_pk_bf16_f32 v71, v72, v73
	ds_write_b128 v44, v[68:71] offset:32768
	v_cndmask_b32_e32 v68, 0, v67, vcc
	v_ldexp_f32 v68, v74, v68
	s_waitcnt vmcnt(1)
	v_lshlrev_b32_e32 v70, 16, v6
	v_and_b32_e32 v71, 0xffff0000, v6
	v_pk_mul_f32 v[70:71], v[68:69], v[70:71] op_sel_hi:[0,1]
	v_cvt_pk_bf16_f32 v6, v70, v71
	v_lshlrev_b32_e32 v70, 16, v7
	v_and_b32_e32 v71, 0xffff0000, v7
	v_pk_mul_f32 v[70:71], v[68:69], v[70:71] op_sel_hi:[0,1]
	v_cvt_pk_bf16_f32 v7, v70, v71
	v_lshlrev_b32_e32 v70, 16, v8
	v_and_b32_e32 v71, 0xffff0000, v8
	v_pk_mul_f32 v[70:71], v[68:69], v[70:71] op_sel_hi:[0,1]
	v_cvt_pk_bf16_f32 v8, v70, v71
	v_lshlrev_b32_e32 v70, 16, v9
	v_and_b32_e32 v71, 0xffff0000, v9
	v_mul_f32_e32 v9, s0, v50
	v_cmp_gt_f32_e32 vcc, s14, v9
	v_pk_mul_f32 v[68:69], v[68:69], v[70:71] op_sel_hi:[0,1]
	s_nop 0
	v_cndmask_b32_e32 v9, 0, v65, vcc
	v_fmac_f32_e32 v9, s0, v50
	v_exp_f32_e32 v70, v9
	v_cvt_pk_bf16_f32 v9, v68, v69
	ds_write_b128 v45, v[6:9] offset:32768
	v_cndmask_b32_e32 v6, 0, v67, vcc
	v_ldexp_f32 v6, v70, v6
	s_waitcnt vmcnt(0)
	v_lshlrev_b32_e32 v8, 16, v2
	v_and_b32_e32 v9, 0xffff0000, v2
	v_pk_mul_f32 v[8:9], v[6:7], v[8:9] op_sel_hi:[0,1]
	v_cvt_pk_bf16_f32 v2, v8, v9
	v_lshlrev_b32_e32 v8, 16, v3
	v_and_b32_e32 v9, 0xffff0000, v3
	v_pk_mul_f32 v[8:9], v[6:7], v[8:9] op_sel_hi:[0,1]
	v_cvt_pk_bf16_f32 v3, v8, v9
	v_lshlrev_b32_e32 v8, 16, v4
	v_and_b32_e32 v9, 0xffff0000, v4
	v_pk_mul_f32 v[8:9], v[6:7], v[8:9] op_sel_hi:[0,1]
	v_cvt_pk_bf16_f32 v4, v8, v9
	v_lshlrev_b32_e32 v8, 16, v5
	v_and_b32_e32 v9, 0xffff0000, v5
	v_pk_mul_f32 v[6:7], v[6:7], v[8:9] op_sel_hi:[0,1]
	v_cvt_pk_bf16_f32 v5, v6, v7
	ds_write_b128 v51, v[2:5] offset:32768
	s_waitcnt lgkmcnt(0)
	s_barrier
	ds_read_b64_tr_b16 v[2:3], v52 offset:32768
	ds_read_b64_tr_b16 v[4:5], v53 offset:32768
	ds_read_b64_tr_b16 v[6:7], v54 offset:32768
	ds_read_b64_tr_b16 v[8:9], v55 offset:32768
	ds_read_b64_tr_b16 v[68:69], v116
	ds_read_b64_tr_b16 v[70:71], v117
	ds_read_b64_tr_b16 v[72:73], v118
	ds_read_b64_tr_b16 v[74:75], v119
	ds_read_b64_tr_b16 v[76:77], v120
	ds_read_b64_tr_b16 v[78:79], v121
	ds_read_b64_tr_b16 v[80:81], v122
	ds_read_b64_tr_b16 v[82:83], v123
	ds_read_b64_tr_b16 v[84:85], v124
	ds_read_b64_tr_b16 v[86:87], v125
	ds_read_b64_tr_b16 v[88:89], v126
	ds_read_b64_tr_b16 v[90:91], v127
	ds_read_b64_tr_b16 v[92:93], v128
	ds_read_b64_tr_b16 v[94:95], v129
	ds_read_b64_tr_b16 v[96:97], v130
	ds_read_b64_tr_b16 v[98:99], v131
	s_waitcnt lgkmcnt(14)
	v_mfma_f32_16x16x32_bf16 v[100:103], v[68:71], v[2:5], 0
	v_mfma_f32_16x16x32_bf16 v[68:71], v[68:71], v[6:9], 0
	s_waitcnt lgkmcnt(12)
	v_mfma_f32_16x16x32_bf16 v[104:107], v[72:75], v[2:5], 0
	v_mfma_f32_16x16x32_bf16 v[72:75], v[72:75], v[6:9], 0
	s_waitcnt lgkmcnt(10)
	v_mfma_f32_16x16x32_bf16 v[108:111], v[76:79], v[2:5], 0
	v_mfma_f32_16x16x32_bf16 v[76:79], v[76:79], v[6:9], 0
	s_waitcnt lgkmcnt(8)
	v_mfma_f32_16x16x32_bf16 v[112:115], v[80:83], v[2:5], 0
	v_mfma_f32_16x16x32_bf16 v[80:83], v[80:83], v[6:9], 0
	s_waitcnt lgkmcnt(6)
	v_mfma_f32_16x16x32_bf16 v[132:135], v[84:87], v[2:5], 0
	v_mfma_f32_16x16x32_bf16 v[84:87], v[84:87], v[6:9], 0
	s_waitcnt lgkmcnt(4)
	v_mfma_f32_16x16x32_bf16 v[136:139], v[88:91], v[2:5], 0
	v_mfma_f32_16x16x32_bf16 v[88:91], v[88:91], v[6:9], 0
	s_waitcnt lgkmcnt(2)
	v_mfma_f32_16x16x32_bf16 v[140:143], v[92:95], v[2:5], 0
	v_mfma_f32_16x16x32_bf16 v[92:95], v[92:95], v[6:9], 0
	s_waitcnt lgkmcnt(0)
; #define MFMA16(a, b, c) __builtin_amdgcn_mfma_f32_16x16x32_bf16(a, b, c, 0, 0, 0)
; __device__ __forceinline__ void kv_unit(Frame& F, const Args& a, int c, int h) {
;     ...
; #pragma unroll
;         for (int ks = 0; ks < 4; ++ks) {
;             const bf16x8 y0 = trf(vi, vb[0][0], vb[0][1], 8192 * ks), y1 = trf(vi, vb[1][0], vb[1][1], 8192 * ks);
;             bf16x8 xf[8];
; #pragma unroll
;             for (int cd = 0; cd < 8; ++cd) xf[cd] = trf(Kimg, kb[cd][0], kb[cd][1], 8192 * ks);
;             __builtin_amdgcn_sched_barrier(0);
; #pragma unroll
;             for (int cd = 0; cd < 8; ++cd) { acc[0][cd] = MFMA16(xf[cd], y0, acc[0][cd]); acc[1][cd] = MFMA16(xf[cd], y1, acc[1][cd]); }
;             __builtin_amdgcn_sched_barrier(0);
;         }
	v_mfma_f32_16x16x32_bf16 v[2:5], v[96:99], v[2:5], 0
	v_mfma_f32_16x16x32_bf16 v[6:9], v[96:99], v[6:9], 0
	ds_read_b64_tr_b16 v[96:97], v52 offset:40960
	ds_read_b64_tr_b16 v[98:99], v53 offset:40960
	ds_read_b64_tr_b16 v[144:145], v54 offset:40960
	ds_read_b64_tr_b16 v[146:147], v55 offset:40960
	ds_read_b64_tr_b16 v[148:149], v116 offset:8192
	ds_read_b64_tr_b16 v[150:151], v117 offset:8192
	ds_read_b64_tr_b16 v[152:153], v118 offset:8192
	ds_read_b64_tr_b16 v[154:155], v119 offset:8192
	ds_read_b64_tr_b16 v[156:157], v120 offset:8192
	ds_read_b64_tr_b16 v[158:159], v121 offset:8192
	ds_read_b64_tr_b16 v[160:161], v122 offset:8192
	ds_read_b64_tr_b16 v[162:163], v123 offset:8192
	ds_read_b64_tr_b16 v[164:165], v124 offset:8192
	ds_read_b64_tr_b16 v[166:167], v125 offset:8192
	ds_read_b64_tr_b16 v[168:169], v126 offset:8192
	ds_read_b64_tr_b16 v[170:171], v127 offset:8192
	ds_read_b64_tr_b16 v[172:173], v128 offset:8192
	ds_read_b64_tr_b16 v[174:175], v129 offset:8192
	ds_read_b64_tr_b16 v[176:177], v130 offset:8192
	ds_read_b64_tr_b16 v[178:179], v131 offset:8192
	s_waitcnt lgkmcnt(14)
	v_mfma_f32_16x16x32_bf16 v[100:103], v[148:151], v[96:99], v[100:103]
	v_mfma_f32_16x16x32_bf16 v[68:71], v[148:151], v[144:147], v[68:71]
	s_waitcnt lgkmcnt(12)
	v_mfma_f32_16x16x32_bf16 v[104:107], v[152:155], v[96:99], v[104:107]
	v_mfma_f32_16x16x32_bf16 v[72:75], v[152:155], v[144:147], v[72:75]
	s_waitcnt lgkmcnt(10)
	v_mfma_f32_16x16x32_bf16 v[108:111], v[156:159], v[96:99], v[108:111]
	v_mfma_f32_16x16x32_bf16 v[76:79], v[156:159], v[144:147], v[76:79]
	s_waitcnt lgkmcnt(8)
	v_mfma_f32_16x16x32_bf16 v[112:115], v[160:163], v[96:99], v[112:115]
	v_mfma_f32_16x16x32_bf16 v[80:83], v[160:163], v[144:147], v[80:83]
	s_waitcnt lgkmcnt(6)
	v_mfma_f32_16x16x32_bf16 v[132:135], v[164:167], v[96:99], v[132:135]
	v_mfma_f32_16x16x32_bf16 v[84:87], v[164:167], v[144:147], v[84:87]
	s_waitcnt lgkmcnt(4)
	v_mfma_f32_16x16x32_bf16 v[136:139], v[168:171], v[96:99], v[136:139]
	v_mfma_f32_16x16x32_bf16 v[88:91], v[168:171], v[144:147], v[88:91]
	s_waitcnt lgkmcnt(2)
	v_mfma_f32_16x16x32_bf16 v[140:143], v[172:175], v[96:99], v[140:143]
	v_mfma_f32_16x16x32_bf16 v[92:95], v[172:175], v[144:147], v[92:95]
	s_waitcnt lgkmcnt(0)
	v_mfma_f32_16x16x32_bf16 v[2:5], v[176:179], v[96:99], v[2:5]
	v_mfma_f32_16x16x32_bf16 v[6:9], v[176:179], v[144:147], v[6:9]
	ds_read_b64_tr_b16 v[96:97], v52 offset:49152
	ds_read_b64_tr_b16 v[98:99], v53 offset:49152
	ds_read_b64_tr_b16 v[144:145], v54 offset:49152
	ds_read_b64_tr_b16 v[146:147], v55 offset:49152
	ds_read_b64_tr_b16 v[148:149], v116 offset:16384
	ds_read_b64_tr_b16 v[150:151], v117 offset:16384
	ds_read_b64_tr_b16 v[152:153], v118 offset:16384
	ds_read_b64_tr_b16 v[154:155], v119 offset:16384
	ds_read_b64_tr_b16 v[156:157], v120 offset:16384
	ds_read_b64_tr_b16 v[158:159], v121 offset:16384
	ds_read_b64_tr_b16 v[160:161], v122 offset:16384
	ds_read_b64_tr_b16 v[162:163], v123 offset:16384
	ds_read_b64_tr_b16 v[164:165], v124 offset:16384
	ds_read_b64_tr_b16 v[166:167], v125 offset:16384
	ds_read_b64_tr_b16 v[168:169], v126 offset:16384
	ds_read_b64_tr_b16 v[170:171], v127 offset:16384
	ds_read_b64_tr_b16 v[172:173], v128 offset:16384
	ds_read_b64_tr_b16 v[174:175], v129 offset:16384
	ds_read_b64_tr_b16 v[176:177], v130 offset:16384
	ds_read_b64_tr_b16 v[178:179], v131 offset:16384
	s_waitcnt lgkmcnt(14)
	v_mfma_f32_16x16x32_bf16 v[100:103], v[148:151], v[96:99], v[100:103]
	v_mfma_f32_16x16x32_bf16 v[68:71], v[148:151], v[144:147], v[68:71]
	s_waitcnt lgkmcnt(12)
	v_mfma_f32_16x16x32_bf16 v[104:107], v[152:155], v[96:99], v[104:107]
	v_mfma_f32_16x16x32_bf16 v[72:75], v[152:155], v[144:147], v[72:75]
	s_waitcnt lgkmcnt(10)
	v_mfma_f32_16x16x32_bf16 v[108:111], v[156:159], v[96:99], v[108:111]
	v_mfma_f32_16x16x32_bf16 v[76:79], v[156:159], v[144:147], v[76:79]
	s_waitcnt lgkmcnt(8)
	v_mfma_f32_16x16x32_bf16 v[112:115], v[160:163], v[96:99], v[112:115]
	v_mfma_f32_16x16x32_bf16 v[80:83], v[160:163], v[144:147], v[80:83]
	s_waitcnt lgkmcnt(6)
	v_mfma_f32_16x16x32_bf16 v[132:135], v[164:167], v[96:99], v[132:135]
	v_mfma_f32_16x16x32_bf16 v[84:87], v[164:167], v[144:147], v[84:87]
	s_waitcnt lgkmcnt(4)
	v_mfma_f32_16x16x32_bf16 v[136:139], v[168:171], v[96:99], v[136:139]
	v_mfma_f32_16x16x32_bf16 v[88:91], v[168:171], v[144:147], v[88:91]
	s_waitcnt lgkmcnt(2)
	v_mfma_f32_16x16x32_bf16 v[140:143], v[172:175], v[96:99], v[140:143]
	v_mfma_f32_16x16x32_bf16 v[92:95], v[172:175], v[144:147], v[92:95]
	s_waitcnt lgkmcnt(0)
; #define LAS __attribute__((address_space(3)))
; __device__ __forceinline__ unsigned cvt_pk_bf16(float lo, float hi) { f32x2 v = {lo, hi}; bf16x2_t b = __builtin_convertvector(v, bf16x2_t); return __builtin_bit_cast(unsigned, b); }
; #define MFMA16(a, b, c) __builtin_amdgcn_mfma_f32_16x16x32_bf16(a, b, c, 0, 0, 0)
; __device__ __forceinline__ void kv_unit(Frame& F, const Args& a, int c, int h) {
;     ...
;             for (int cd = 0; cd < 8; ++cd) xf[cd] = trf(Kimg, kb[cd][0], kb[cd][1], 8192 * ks);
;             __builtin_amdgcn_sched_barrier(0);
; #pragma unroll
;             for (int cd = 0; cd < 8; ++cd) { acc[0][cd] = MFMA16(xf[cd], y0, acc[0][cd]); acc[1][cd] = MFMA16(xf[cd], y1, acc[1][cd]); }
;             __builtin_amdgcn_sched_barrier(0);
;         }
;     }
;     bf16_t* out = (bf16_t*)KV + (size_t)(c * 8 + h) * 32768;
;     __syncthreads();
;     LAS unsigned char* KT = F.lds;
; #pragma unroll
;     for (int j = 0; j < 2; ++j)
; #pragma unroll
;         for (int cd = 0; cd < 8; ++cd) { const int e = 16 * (2 * w + j) + (lane & 15), d = 16 * cd + 4 * (lane >> 4);
;             u32x2 o; o.x = cvt_pk_bf16(acc[j][cd][0], acc[j][cd][1]); o.y = cvt_pk_bf16(acc[j][cd][2], acc[j][cd][3]); *(LAS u32x2*)(KT + e * 272 + d * 2) = o; }
;     __syncthreads();
; #pragma unroll
;     for (int i = 0; i < 8; ++i) { const int id = tid + 512 * i, e = id >> 4, ch = id & 15;
;         *(u32x4*)(out + e * 128 + 8 * ch) = *(const LAS u32x4*)(KT + e * 272 + 16 * ch); }
;     __syncthreads();
; __global__ void __launch_bounds__(NTHREADS, 2) mk_fwd(Args args) {
;     ...
;         for (int u = blockIdx.x; u < 1024; u += F.G) kv_unit(F, args, u >> 3, u & 7);
	v_mfma_f32_16x16x32_bf16 v[2:5], v[176:179], v[96:99], v[2:5]
	v_mfma_f32_16x16x32_bf16 v[6:9], v[176:179], v[144:147], v[6:9]
	ds_read_b64_tr_b16 v[96:97], v52 offset:57344
	ds_read_b64_tr_b16 v[98:99], v53 offset:57344
	ds_read_b64_tr_b16 v[144:145], v54 offset:57344
	ds_read_b64_tr_b16 v[146:147], v55 offset:57344
	ds_read_b64_tr_b16 v[148:149], v116 offset:24576
	ds_read_b64_tr_b16 v[150:151], v117 offset:24576
	ds_read_b64_tr_b16 v[152:153], v118 offset:24576
	ds_read_b64_tr_b16 v[154:155], v119 offset:24576
	ds_read_b64_tr_b16 v[156:157], v120 offset:24576
	ds_read_b64_tr_b16 v[158:159], v121 offset:24576
	ds_read_b64_tr_b16 v[160:161], v122 offset:24576
	ds_read_b64_tr_b16 v[162:163], v123 offset:24576
	ds_read_b64_tr_b16 v[164:165], v124 offset:24576
	ds_read_b64_tr_b16 v[166:167], v125 offset:24576
	ds_read_b64_tr_b16 v[168:169], v126 offset:24576
	ds_read_b64_tr_b16 v[170:171], v127 offset:24576
	ds_read_b64_tr_b16 v[172:173], v128 offset:24576
	ds_read_b64_tr_b16 v[174:175], v129 offset:24576
	ds_read_b64_tr_b16 v[176:177], v130 offset:24576
	ds_read_b64_tr_b16 v[178:179], v131 offset:24576
	s_waitcnt lgkmcnt(14)
	v_mfma_f32_16x16x32_bf16 v[100:103], v[148:151], v[96:99], v[100:103]
	v_mfma_f32_16x16x32_bf16 v[68:71], v[148:151], v[144:147], v[68:71]
	s_waitcnt lgkmcnt(12)
	v_mfma_f32_16x16x32_bf16 v[104:107], v[152:155], v[96:99], v[104:107]
	v_mfma_f32_16x16x32_bf16 v[72:75], v[152:155], v[144:147], v[72:75]
	s_waitcnt lgkmcnt(10)
	v_mfma_f32_16x16x32_bf16 v[108:111], v[156:159], v[96:99], v[108:111]
	v_mfma_f32_16x16x32_bf16 v[76:79], v[156:159], v[144:147], v[76:79]
	s_waitcnt lgkmcnt(8)
	v_mfma_f32_16x16x32_bf16 v[112:115], v[160:163], v[96:99], v[112:115]
	v_mfma_f32_16x16x32_bf16 v[80:83], v[160:163], v[144:147], v[80:83]
	s_waitcnt lgkmcnt(6)
	v_mfma_f32_16x16x32_bf16 v[132:135], v[164:167], v[96:99], v[132:135]
	v_mfma_f32_16x16x32_bf16 v[84:87], v[164:167], v[144:147], v[84:87]
	s_waitcnt lgkmcnt(4)
	v_mfma_f32_16x16x32_bf16 v[136:139], v[168:171], v[96:99], v[136:139]
	v_mfma_f32_16x16x32_bf16 v[88:91], v[168:171], v[144:147], v[88:91]
	s_waitcnt lgkmcnt(2)
	v_mfma_f32_16x16x32_bf16 v[140:143], v[172:175], v[96:99], v[140:143]
	v_mfma_f32_16x16x32_bf16 v[92:95], v[172:175], v[144:147], v[92:95]
	s_waitcnt lgkmcnt(0)
	v_mfma_f32_16x16x32_bf16 v[2:5], v[176:179], v[96:99], v[2:5]
	v_mfma_f32_16x16x32_bf16 v[6:9], v[176:179], v[144:147], v[6:9]
	v_cvt_pk_bf16_f32 v96, v100, v101
	v_cvt_pk_bf16_f32 v97, v102, v103
	v_cvt_pk_bf16_f32 v98, v104, v105
	v_cvt_pk_bf16_f32 v99, v106, v107
	s_nop 2
	v_cvt_pk_bf16_f32 v2, v2, v3
	v_cvt_pk_bf16_f32 v3, v4, v5
	v_cvt_pk_bf16_f32 v4, v68, v69
	v_cvt_pk_bf16_f32 v5, v70, v71
	v_cvt_pk_bf16_f32 v68, v72, v73
	v_cvt_pk_bf16_f32 v69, v74, v75
	v_cvt_pk_bf16_f32 v70, v76, v77
	v_cvt_pk_bf16_f32 v71, v78, v79
	v_cvt_pk_bf16_f32 v72, v80, v81
	v_cvt_pk_bf16_f32 v73, v82, v83
	v_cvt_pk_bf16_f32 v74, v84, v85
	v_cvt_pk_bf16_f32 v75, v86, v87
	v_cvt_pk_bf16_f32 v76, v88, v89
	v_cvt_pk_bf16_f32 v77, v90, v91
	v_cvt_pk_bf16_f32 v78, v92, v93
	v_cvt_pk_bf16_f32 v79, v94, v95
	v_cvt_pk_bf16_f32 v6, v6, v7
	v_cvt_pk_bf16_f32 v7, v8, v9
	s_barrier
	v_cvt_pk_bf16_f32 v100, v108, v109
	v_cvt_pk_bf16_f32 v101, v110, v111
	v_cvt_pk_bf16_f32 v102, v112, v113
	v_cvt_pk_bf16_f32 v103, v114, v115
	v_cvt_pk_bf16_f32 v104, v132, v133
	v_cvt_pk_bf16_f32 v105, v134, v135
	v_cvt_pk_bf16_f32 v106, v136, v137
	v_cvt_pk_bf16_f32 v107, v138, v139
	v_cvt_pk_bf16_f32 v108, v140, v141
	v_cvt_pk_bf16_f32 v109, v142, v143
	v_add_u32_e32 v138, 0x1000, v56
	ds_write2_b64 v56, v[96:97], v[98:99] offset1:4
	ds_write2_b64 v56, v[100:101], v[102:103] offset0:8 offset1:12
	ds_write2_b64 v56, v[104:105], v[106:107] offset0:16 offset1:20
	ds_write2_b64 v56, v[108:109], v[2:3] offset0:24 offset1:28
	ds_write2_b64 v138, v[4:5], v[68:69] offset0:32 offset1:36
	ds_write2_b64 v138, v[70:71], v[72:73] offset0:40 offset1:44
	ds_write2_b64 v138, v[74:75], v[76:77] offset0:48 offset1:52
	ds_write2_b64 v138, v[78:79], v[6:7] offset0:56 offset1:60
	s_waitcnt lgkmcnt(0)
	s_barrier
	ds_read_b128 v[2:5], v57
	ds_read_b128 v[6:9], v58
	ds_read_b128 v[68:71], v59
	ds_read_b128 v[72:75], v60
	ds_read_b128 v[76:79], v61
	ds_read_b128 v[80:83], v62
	ds_read_b128 v[84:87], v63
	ds_read_b128 v[88:91], v64
	s_add_i32 s15, s15, s4
	s_add_i32 s33, s33, s90
	v_lshl_add_u64 v[92:93], v[16:17], 0, v[14:15]
	v_lshl_add_u64 v[94:95], v[16:17], 0, v[18:19]
	v_lshl_add_u64 v[110:111], v[16:17], 0, v[20:21]
	v_lshl_add_u64 v[112:113], v[16:17], 0, v[22:23]
	v_lshl_add_u64 v[114:115], v[16:17], 0, v[24:25]
	v_lshl_add_u64 v[132:133], v[16:17], 0, v[26:27]
	v_lshl_add_u64 v[134:135], v[16:17], 0, v[28:29]
	v_lshl_add_u64 v[136:137], v[16:17], 0, v[30:31]
	v_lshl_add_u64 v[16:17], v[16:17], 0, s[6:7]
	s_cmp_lt_i32 s15, s99
	s_waitcnt lgkmcnt(7)
	global_store_dwordx4 v[92:93], v[2:5], off
	s_waitcnt lgkmcnt(6)
	global_store_dwordx4 v[94:95], v[6:9], off
	s_waitcnt lgkmcnt(5)
	global_store_dwordx4 v[110:111], v[68:71], off
	s_waitcnt lgkmcnt(4)
	global_store_dwordx4 v[112:113], v[72:75], off
	s_waitcnt lgkmcnt(3)
	global_store_dwordx4 v[114:115], v[76:79], off
	s_waitcnt lgkmcnt(2)
	global_store_dwordx4 v[132:133], v[80:83], off
	s_waitcnt lgkmcnt(1)
	global_store_dwordx4 v[134:135], v[84:87], off
	s_waitcnt lgkmcnt(0)
	global_store_dwordx4 v[136:137], v[88:91], off
	s_barrier
	s_cbranch_scc1 .LBB0_351
	v_readlane_b32 s92, v254, 12
	s_load_dwordx2 s[88:89], s[96:97], 0xc0
	s_movk_i32 s2, 0x100
	v_readlane_b32 s4, v254, 10
	v_readlane_b32 s5, v254, 11
